# baseline (speedup 1.0000x reference)
.LBB0_7:
	s_add_i32 s95, s82, -1
	s_lshl_b32 s90, s91, 6
	s_add_i32 s96, s3, -1
	s_add_i32 s88, s89, s33
	s_cmp_lg_u32 s85, 0
	s_cbranch_scc1 .Litem_loaded
	v_mov_b32_e32 v2, v0
	s_add_i32 s95, s82, -1
	s_lshl_b32 s90, s91, 6
	v_ashrrev_i32_e32 v52, 4, v2
	v_bfe_u32 v53, v2, 4, 2
	v_lshlrev_b32_e32 v2, 2, v2
	s_cmp_gt_i32 s82, 1
	v_and_or_b32 v2, v2, 60, s90
	s_cselect_b32 s4, 64, 0
	s_add_i32 s96, s3, -1
	v_lshlrev_b64 v[4:5], 2, v[2:3]
	v_min_i32_e32 v2, s96, v52
	v_add_lshl_u32 v2, v2, s76, 10
	v_lshlrev_b64 v[8:9], 2, v[2:3]
	v_add_u32_e32 v2, 32, v52
	v_min_i32_e32 v2, s96, v2
	s_waitcnt lgkmcnt(0)
	v_lshl_add_u64 v[6:7], s[70:71], 0, v[4:5]
	v_add_lshl_u32 v2, v2, s76, 10
	v_lshl_add_u64 v[10:11], v[6:7], 0, v[8:9]
	v_lshlrev_b64 v[12:13], 2, v[2:3]
	v_lshl_add_u64 v[14:15], v[6:7], 0, v[12:13]
	global_load_dwordx4 v[70:73], v[10:11], off
	global_load_dwordx4 v[66:69], v[14:15], off
	v_lshl_add_u64 v[10:11], s[74:75], 0, v[4:5]
	v_lshl_add_u64 v[16:17], v[10:11], 0, v[8:9]
	v_lshl_add_u64 v[50:51], v[10:11], 0, v[12:13]
	global_load_dwordx4 v[182:185], v[16:17], off
	global_load_dwordx4 v[186:189], v[50:51], off
	v_add_u32_e32 v50, s4, v52
	v_min_i32_e32 v2, s96, v50
	v_add_lshl_u32 v2, v2, s76, 10
	v_lshl_add_u64 v[16:17], v[2:3], 2, v[6:7]
	v_add_u32_e32 v2, 32, v50
	v_min_i32_e32 v2, s96, v2
	v_add_lshl_u32 v2, v2, s76, 10
	s_min_i32 s5, s95, 2
	v_lshl_add_u64 v[50:51], v[2:3], 2, v[6:7]
	global_load_dwordx4 v[90:93], v[16:17], off
	global_load_dwordx4 v[82:85], v[50:51], off
	v_lshl_add_u32 v50, s5, 6, v52
	v_min_i32_e32 v2, s96, v50
	v_add_lshl_u32 v2, v2, s76, 10
	v_lshl_add_u64 v[16:17], v[2:3], 2, v[6:7]
	v_add_u32_e32 v2, 32, v50
	v_min_i32_e32 v2, s96, v2
	s_add_i32 s88, s89, s33
	v_add_lshl_u32 v2, v2, s76, 10
	v_add_u32_e32 v54, s88, v53
	v_lshl_add_u64 v[6:7], v[2:3], 2, v[6:7]
	v_min_i32_e32 v2, s96, v54
	v_lshl_add_u64 v[4:5], s[68:69], 0, v[4:5]
	v_add_lshl_u32 v2, v2, s76, 10
	global_load_dwordx4 v[98:101], v[16:17], off
	global_load_dwordx4 v[94:97], v[6:7], off
	v_lshl_add_u64 v[6:7], v[2:3], 2, v[4:5]
	v_add_u32_e32 v2, 4, v54
	v_min_i32_e32 v2, s96, v2
	v_add_lshl_u32 v2, v2, s76, 10
	v_lshl_add_u64 v[16:17], v[2:3], 2, v[4:5]
	v_add_u32_e32 v2, 8, v54
	v_min_i32_e32 v2, s96, v2
	v_add_lshl_u32 v2, v2, s76, 10
	global_load_dwordx4 v[86:89], v[6:7], off nt
	global_load_dwordx4 v[74:77], v[16:17], off nt
	v_lshl_add_u64 v[6:7], v[2:3], 2, v[4:5]
	v_add_u32_e32 v2, 12, v54
	v_min_i32_e32 v2, s96, v2
	v_add_lshl_u32 v2, v2, s76, 10
	v_lshl_add_u64 v[16:17], v[2:3], 2, v[4:5]
	v_add_u32_e32 v2, 16, v54
	v_min_i32_e32 v2, s96, v2
	v_add_lshl_u32 v2, v2, s76, 10
	global_load_dwordx4 v[78:81], v[6:7], off nt
	global_load_dwordx4 v[58:61], v[16:17], off nt
	v_lshl_add_u64 v[6:7], v[2:3], 2, v[4:5]
	v_add_u32_e32 v2, 20, v54
	v_min_i32_e32 v2, s96, v2
	v_add_lshl_u32 v2, v2, s76, 10
	v_lshl_add_u64 v[16:17], v[2:3], 2, v[4:5]
	v_add_u32_e32 v2, 24, v54
	v_min_i32_e32 v2, s96, v2
	v_add_lshl_u32 v2, v2, s76, 10
	global_load_dwordx4 v[62:65], v[6:7], off nt
	global_load_dwordx4 v[50:53], v[16:17], off nt
	v_lshl_add_u64 v[16:17], v[2:3], 2, v[4:5]
	v_add_u32_e32 v2, 28, v54
	v_min_i32_e32 v2, s96, v2
	v_add_lshl_u32 v2, v2, s76, 10
	v_lshl_add_u64 v[102:103], v[2:3], 2, v[4:5]
	global_load_dwordx4 v[54:57], v[16:17], off nt
	global_load_dwordx4 v[178:181], v[102:103], off nt
.Litem_loaded:
	s_cmp_eq_u32 s85, 0
	s_cselect_b64 s[4:5], -1, 0
	s_and_b64 s[8:9], s[4:5], s[0:1]
	s_and_saveexec_b64 s[6:7], s[8:9]
	s_cbranch_execz .LBB0_11
	global_load_ubyte v2, v[226:227], off
	s_movk_i32 s8, 0xff
	v_mov_b32_e32 v102, 0
	v_mov_b32_e32 v103, 0
	v_mov_b32_e32 v104, 0
	v_mov_b32_e32 v105, 0
	s_waitcnt vmcnt(0)
	v_cmp_ne_u16_e32 vcc, s8, v2
	s_and_saveexec_b64 s[8:9], vcc
	s_cbranch_execz .LBB0_10
	v_and_b32_sdwa v16, v2, v240 dst_sel:DWORD dst_unused:UNUSED_PAD src0_sel:WORD_0 src1_sel:DWORD
	v_readlane_b32 s16, v255, 0
	v_lshlrev_b32_e32 v16, 2, v16
	v_readlane_b32 s17, v255, 1
	s_nop 4
	global_load_dwordx2 v[102:103], v16, s[16:17]
	v_add_u32_sdwa v16, s2, v2 dst_sel:DWORD dst_unused:UNUSED_PAD src0_sel:DWORD src1_sel:WORD_0
	v_lshlrev_b32_sdwa v2, v241, v2 dst_sel:DWORD dst_unused:UNUSED_PAD src0_sel:DWORD src1_sel:WORD_0
	v_and_or_b32 v16, v16, 7, s67
	v_and_b32_e32 v2, 0xf00, v2
	v_lshl_or_b32 v104, v16, 16, v2
	s_waitcnt vmcnt(0)
	v_sub_u32_e32 v103, v103, v102
	v_add_u32_e32 v2, 63, v103
	v_ashrrev_i32_e32 v16, 31, v2
	v_lshrrev_b32_e32 v16, 26, v16
	v_add_u32_e32 v2, v2, v16
	v_ashrrev_i32_e32 v105, 6, v2

.LBB0_11:
	s_or_b64 exec, exec, s[6:7]
	v_mov_b32_e32 v2, v0
	s_waitcnt vmcnt(14)
	v_cvt_pkrtz_f16_f32 v66, v66, v67
	v_bfe_u32 v17, v2, 1, 3
	v_lshrrev_b32_e32 v103, 5, v2
	v_ashrrev_i32_e32 v102, 4, v2
	v_bitop3_b32 v17, v17, v103, 7 bitop3:0x78
	v_lshlrev_b32_e32 v103, 3, v2
	v_lshlrev_b32_e32 v16, 7, v102
	v_lshlrev_b32_e32 v17, 4, v17
	v_and_b32_e32 v104, 8, v103
	v_or3_b32 v104, v16, v17, v104
	v_cvt_pkrtz_f16_f32 v16, v70, v71
	v_cvt_pkrtz_f16_f32 v17, v72, v73
	v_cvt_pkrtz_f16_f32 v67, v68, v69
	ds_write2st64_b64 v104, v[16:17], v[66:67] offset1:8
	s_waitcnt vmcnt(11)
	v_cvt_pkrtz_f16_f32 v16, v90, v91
	v_cvt_pkrtz_f16_f32 v17, v92, v93
	s_waitcnt vmcnt(10)
	v_cvt_pkrtz_f16_f32 v66, v82, v83
	v_cvt_pkrtz_f16_f32 v67, v84, v85
	ds_write2st64_b64 v104, v[16:17], v[66:67] offset0:16 offset1:24
	s_waitcnt vmcnt(9)
	v_cvt_pkrtz_f16_f32 v16, v98, v99
	v_cvt_pkrtz_f16_f32 v17, v100, v101
	s_waitcnt vmcnt(8)
	v_cvt_pkrtz_f16_f32 v66, v94, v95
	v_cvt_pkrtz_f16_f32 v67, v96, v97
	ds_write2st64_b64 v104, v[16:17], v[66:67] offset0:32 offset1:40
	v_bfe_u32 v2, v2, 3, 1
	v_lshlrev_b32_e32 v16, 6, v102
	v_mad_u32_u24 v2, v2, s86, v16
	v_and_or_b32 v2, v103, 56, v2
	v_cvt_pkrtz_f16_f32 v12, v182, v183
	v_cvt_pkrtz_f16_f32 v13, v184, v185
	v_cvt_pkrtz_f16_f32 v8, v186, v187
	v_cvt_pkrtz_f16_f32 v9, v188, v189
	ds_write2st64_b64 v2, v[12:13], v[8:9] offset0:48 offset1:52
	v_mov_b32_e32 v2, v229
	s_waitcnt vmcnt(7)
	v_pk_mul_f32 v[10:11], v[86:87], s[78:79] op_sel_hi:[1,0]
	v_lshlrev_b32_e32 v8, 3, v2
	v_ashrrev_i32_e32 v14, 4, v2
	v_and_b32_e32 v15, 8, v8
	v_pk_mul_f32 v[8:9], v[88:89], s[78:79] op_sel_hi:[1,0]
	v_cvt_pkrtz_f16_f32 v10, v10, v11
	v_cvt_pkrtz_f16_f32 v11, v8, v9
	v_xor_b32_e32 v9, v14, v2
	v_lshlrev_b32_e32 v9, 3, v9
	v_lshl_add_u32 v8, v14, 7, s79
	v_and_b32_e32 v9, 0x70, v9
	v_add3_u32 v16, v8, v9, v15
	v_add_u32_e32 v17, 4, v14
	s_waitcnt vmcnt(6)
	v_pk_mul_f32 v[8:9], v[76:77], s[78:79] op_sel_hi:[1,0]
	v_pk_mul_f32 v[12:13], v[74:75], s[78:79] op_sel_hi:[1,0]
	s_waitcnt vmcnt(0)
	v_pk_mul_f32 v[6:7], v[180:181], s[78:79] op_sel_hi:[1,0]
	v_cvt_pkrtz_f16_f32 v12, v12, v13
	v_cvt_pkrtz_f16_f32 v13, v8, v9
	v_xor_b32_e32 v9, v17, v2
	v_lshlrev_b32_e32 v9, 3, v9
	v_lshl_add_u32 v8, v17, 7, s79
	v_and_b32_e32 v9, 0x70, v9
	v_add3_u32 v8, v8, v9, v15
	ds_write_b64 v8, v[12:13] offset:41216
	v_add_u32_e32 v17, 8, v14
	v_pk_mul_f32 v[8:9], v[80:81], s[78:79] op_sel_hi:[1,0]
	v_pk_mul_f32 v[12:13], v[78:79], s[78:79] op_sel_hi:[1,0]
	v_pk_mul_f32 v[4:5], v[178:179], s[78:79] op_sel_hi:[1,0]
	v_cvt_pkrtz_f16_f32 v12, v12, v13
	v_cvt_pkrtz_f16_f32 v13, v8, v9
	v_xor_b32_e32 v9, v17, v2
	v_lshlrev_b32_e32 v9, 3, v9
	v_lshl_add_u32 v8, v17, 7, s79
	v_and_b32_e32 v9, 0x70, v9
	v_add3_u32 v8, v8, v9, v15
	ds_write_b64 v8, v[12:13] offset:41216
	v_add_u32_e32 v17, 12, v14
	v_pk_mul_f32 v[8:9], v[60:61], s[78:79] op_sel_hi:[1,0]
	v_pk_mul_f32 v[12:13], v[58:59], s[78:79] op_sel_hi:[1,0]
	v_cvt_pkrtz_f16_f32 v4, v4, v5
	v_cvt_pkrtz_f16_f32 v12, v12, v13
	v_cvt_pkrtz_f16_f32 v13, v8, v9
	v_xor_b32_e32 v9, v17, v2
	v_lshlrev_b32_e32 v9, 3, v9
	v_lshl_add_u32 v8, v17, 7, s79
	v_and_b32_e32 v9, 0x70, v9
	v_add3_u32 v8, v8, v9, v15
	ds_write_b64 v8, v[12:13] offset:41216
	v_pk_mul_f32 v[8:9], v[64:65], s[78:79] op_sel_hi:[1,0]
	v_pk_mul_f32 v[12:13], v[62:63], s[78:79] op_sel_hi:[1,0]
	v_cvt_pkrtz_f16_f32 v5, v6, v7
	v_cvt_pkrtz_f16_f32 v12, v12, v13
	v_cvt_pkrtz_f16_f32 v13, v8, v9
	v_add_u32_e32 v8, 0x100, v16
	ds_write2st64_b64 v8, v[10:11], v[12:13] offset0:80 offset1:84
	v_add_u32_e32 v12, 20, v14
	v_pk_mul_f32 v[8:9], v[52:53], s[78:79] op_sel_hi:[1,0]
	v_pk_mul_f32 v[10:11], v[50:51], s[78:79] op_sel_hi:[1,0]
	s_andn2_b64 vcc, exec, s[4:5]
	v_cvt_pkrtz_f16_f32 v10, v10, v11
	v_cvt_pkrtz_f16_f32 v11, v8, v9
	v_xor_b32_e32 v9, v12, v2
	v_lshlrev_b32_e32 v9, 3, v9
	v_lshl_add_u32 v8, v12, 7, s79
	v_and_b32_e32 v9, 0x70, v9
	v_add3_u32 v8, v8, v9, v15
	ds_write_b64 v8, v[10:11] offset:41216
	v_add_u32_e32 v12, 24, v14
	v_pk_mul_f32 v[8:9], v[56:57], s[78:79] op_sel_hi:[1,0]
	v_pk_mul_f32 v[10:11], v[54:55], s[78:79] op_sel_hi:[1,0]
	s_mov_b32 s94, s11
	v_cvt_pkrtz_f16_f32 v10, v10, v11
	v_cvt_pkrtz_f16_f32 v11, v8, v9
	v_xor_b32_e32 v9, v12, v2
	v_lshlrev_b32_e32 v9, 3, v9
	v_lshl_add_u32 v8, v12, 7, s79
	v_and_b32_e32 v9, 0x70, v9
	v_add3_u32 v8, v8, v9, v15
	ds_write_b64 v8, v[10:11] offset:41216
	v_add_u32_e32 v8, 28, v14
	v_xor_b32_e32 v2, v8, v2
	v_lshlrev_b32_e32 v2, 3, v2
	v_lshl_add_u32 v6, v8, 7, s79
	v_and_b32_e32 v2, 0x70, v2
	v_add3_u32 v2, v6, v2, v15
	s_mov_b32 s91, s13
	s_mov_b32 s89, s14
	s_mov_b32 s93, s12
	s_mov_b32 s92, s10
	ds_write_b64 v2, v[4:5] offset:41216
	s_waitcnt lgkmcnt(0)
	s_barrier
	s_cbranch_vccnz .LBB0_13
	ds_read_b128 v[4:7], v235
	s_waitcnt lgkmcnt(0)
	v_readfirstlane_b32 s4, v6
	v_readfirstlane_b32 s92, v4
	v_readfirstlane_b32 s93, v5
	s_and_b32 s89, s4, 0xffff
	s_ashr_i32 s91, s4, 16
	v_readfirstlane_b32 s94, v7

.LBB0_48:
	s_cmp_eq_u32 s94, 0
	s_cbranch_scc1 .Lno_next
	s_lshl_b32 s44, s92, 12
	s_lshl_b32 s45, s91, 8
	s_add_u32 s44, s44, s45
	s_add_u32 s34, s70, s44
	s_addc_u32 s35, s71, 0
	s_add_u32 s36, s74, s44
	s_addc_u32 s37, s75, 0
	s_add_u32 s38, s68, s44
	s_addc_u32 s39, s69, 0
	s_add_i32 s40, s93, -1
	s_cmp_gt_i32 s94, 1
	s_cselect_b32 s41, 64, 0
	s_add_i32 s42, s94, -1
	s_min_i32 s42, s42, 2
	s_lshl_b32 s42, s42, 6
	s_add_i32 s43, s89, s33
	v_lshrrev_b32_e32 v16, 4, v0
	v_and_b32_e32 v17, 15, v0
	v_lshlrev_b32_e32 v17, 4, v17
	v_bfe_u32 v20, v0, 4, 2
	v_add_u32_e32 v20, s43, v20
	v_min_i32_e32 v18, s40, v16
	v_lshl_add_u32 v18, v18, 12, v17
	global_load_dwordx4 v[70:73], v18, s[34:35]
	v_add_u32_e32 v19, 32, v16
	v_min_i32_e32 v19, s40, v19
	v_lshl_add_u32 v19, v19, 12, v17
	global_load_dwordx4 v[66:69], v19, s[34:35]
	global_load_dwordx4 v[182:185], v18, s[36:37]
	global_load_dwordx4 v[186:189], v19, s[36:37]
	v_add_u32_e32 v21, s41, v16
	v_min_i32_e32 v21, s40, v21
	v_lshl_add_u32 v21, v21, 12, v17
	global_load_dwordx4 v[90:93], v21, s[34:35]
	v_add3_u32 v22, s41, v16, 32
	v_min_i32_e32 v22, s40, v22
	v_lshl_add_u32 v22, v22, 12, v17
	global_load_dwordx4 v[82:85], v22, s[34:35]
	v_add_u32_e32 v18, s42, v16
	v_min_i32_e32 v18, s40, v18
	v_lshl_add_u32 v18, v18, 12, v17
	global_load_dwordx4 v[98:101], v18, s[34:35]
	v_add3_u32 v19, s42, v16, 32
	v_min_i32_e32 v19, s40, v19
	v_lshl_add_u32 v19, v19, 12, v17
	global_load_dwordx4 v[94:97], v19, s[34:35]
	v_min_i32_e32 v21, s40, v20
	v_lshl_add_u32 v21, v21, 12, v17
	global_load_dwordx4 v[86:89], v21, s[38:39] nt
	v_add_u32_e32 v22, 4, v20
	v_min_i32_e32 v22, s40, v22
	v_lshl_add_u32 v22, v22, 12, v17
	global_load_dwordx4 v[74:77], v22, s[38:39] nt
	v_add_u32_e32 v21, 8, v20
	v_min_i32_e32 v21, s40, v21
	v_lshl_add_u32 v21, v21, 12, v17
	global_load_dwordx4 v[78:81], v21, s[38:39] nt
	v_add_u32_e32 v22, 12, v20
	v_min_i32_e32 v22, s40, v22
	v_lshl_add_u32 v22, v22, 12, v17
	global_load_dwordx4 v[58:61], v22, s[38:39] nt
	v_add_u32_e32 v21, 16, v20
	v_min_i32_e32 v21, s40, v21
	v_lshl_add_u32 v21, v21, 12, v17
	global_load_dwordx4 v[62:65], v21, s[38:39] nt
	v_add_u32_e32 v22, 20, v20
	v_min_i32_e32 v22, s40, v22
	v_lshl_add_u32 v22, v22, 12, v17
	global_load_dwordx4 v[50:53], v22, s[38:39] nt
	v_add_u32_e32 v21, 24, v20
	v_min_i32_e32 v21, s40, v21
	v_lshl_add_u32 v21, v21, 12, v17
	global_load_dwordx4 v[54:57], v21, s[38:39] nt
	v_add_u32_e32 v22, 28, v20
	v_min_i32_e32 v22, s40, v22
	v_lshl_add_u32 v22, v22, 12, v17
	global_load_dwordx4 v[178:181], v22, s[38:39] nt
